# cfgE + dense weight conversions (w_out1, w_glu, w_in1) also moved from PRO to the H0-shadow converters
# speedup vs baseline: 1.0180x; 1.0025x over previous
.LBB0_15:
	v_lshlrev_b32_e32 v67, 2, v0
	v_and_b32_e32 v71, 60, v67
	v_bfe_u32 v93, v0, 4, 2
	v_lshlrev_b32_e32 v1, 2, v71
	v_mul_u32_u24_e32 v2, 0x104, v93
	v_add3_u32 v73, v31, v1, v2
	v_lshlrev_b32_e32 v1, 3, v0
	v_and_b32_e32 v2, 56, v1
	v_mul_u32_u24_e32 v3, 0x104, v2
	v_lshlrev_b32_e32 v4, 2, v66
	s_movk_i32 s0, 0x400
	v_mov_b32_e32 v77, 0
	v_add3_u32 v88, v31, v3, v4
	v_or_b32_e32 v89, 32, v66
	v_or_b32_e32 v90, 40, v66
	v_or_b32_e32 v91, 48, v66
	v_or_b32_e32 v92, 56, v66
	v_cmp_gt_i32_e64 s[6:7], s0, v69
	v_lshlrev_b32_e32 v76, 1, v2
	v_lshlrev_b32_e32 v94, 6, v186
	s_cmp_lg_u32 s99, 0
	s_cselect_b64 vcc, s[6:7], 0
	s_and_saveexec_b64 s[0:1], vcc
	s_cbranch_execz .LBB0_50
	v_lshl_add_u64 v[2:3], s[58:59], 0, v[76:77]
	s_mov_b64 s[8:9], 0x3da00000
	v_lshl_add_u64 v[82:83], v[2:3], 0, s[8:9]
	v_lshl_or_b32 v77, s96, 9, v94
	s_lshl_b32 s14, s3, 6
	s_mov_b64 s[8:9], 0
	s_movk_i32 s15, 0x800
	s_movk_i32 s16, 0x3ff
	v_mov_b32_e32 v95, v69
	s_branch .LBB0_18

.LBB0_50:
	s_or_b64 exec, exec, s[0:1]
	s_movk_i32 s0, 0x100
	v_cmp_gt_i32_e32 vcc, s0, v69
	s_cmp_lg_u32 s99, 0
	s_cselect_b64 vcc, vcc, 0
	s_and_saveexec_b64 s[0:1], vcc
	s_cbranch_execz .LBB0_85
	v_mov_b32_e32 v77, 0
	v_lshl_add_u64 v[2:3], s[58:59], 0, v[76:77]
	s_mov_b64 s[8:9], 0x3d800000
	v_lshl_add_u64 v[82:83], v[2:3], 0, s[8:9]
	v_lshl_or_b32 v77, s96, 9, v94
	s_lshl_b32 s14, s3, 6
	s_mov_b64 s[8:9], 0
	s_movk_i32 s15, 0x400
	s_movk_i32 s16, 0xff
	v_mov_b32_e32 v95, v69
	s_branch .LBB0_53

.LBB0_85:
	s_or_b64 exec, exec, s[0:1]
	s_movk_i32 s0, 0xa80
	v_cmp_gt_i32_e32 vcc, s0, v69
	s_cmp_lg_u32 s99, 0
	s_cselect_b64 vcc, vcc, 0
	s_and_saveexec_b64 s[0:1], vcc
	s_cbranch_execz .LBB0_120
	v_mov_b32_e32 v77, 0
	v_lshl_add_u64 v[2:3], s[58:59], 0, v[76:77]
	s_mov_b64 s[8:9], 0x3c300000
	v_lshl_or_b32 v77, s96, 9, v94
	v_lshl_add_u64 v[82:83], v[2:3], 0, s[8:9]
	v_or_b32_e32 v2, v77, v93
	s_movk_i32 s17, 0x1410
	s_lshl_b32 s16, s3, 6
	v_mul_lo_u32 v84, v2, s17
	s_mul_i32 s18, s3, 0x50400
	s_mov_b64 s[12:13], 0
	s_mov_b32 s19, 0xff5f8000
	s_movk_i32 s21, 0xa7f
	v_mov_b32_e32 v85, v69
	s_branch .LBB0_88
